# GEMM pipeline fill: all seven prologue stages issued back to back (the lagging half's extra barrier moved behind them); one prologue barrier less
# baseline (speedup 1.0000x reference)
.LBB0_415:
	v_and_b32_e32 v9, 15, v8
	v_and_b32_e32 v18, 48, v8
	v_lshlrev_b32_e32 v8, 2, v8
	v_mov_b32_e32 v155, v131
	s_sext_i32_i8 s17, s6
	s_and_b32 s8, s8, 3
	v_lshl_or_b32 v19, s7, 6, v9
	s_lshl_b32 s6, s7, 13
	v_lshl_or_b32 v9, v9, 6, v18
	v_and_b32_e32 v8, 32, v8
	v_lshl_add_u64 v[10:11], s[68:69], 0, v[154:155]
	v_mov_b32_e32 v151, v131
	v_bitop3_b32 v20, v9, s6, v8 bitop3:0xde
	s_lshl_b32 s6, s8, 12
	v_lshl_add_u64 v[12:13], s[68:69], 0, v[150:151]
	v_mov_b32_e32 v153, v131
	v_bitop3_b32 v168, v9, s6, v8 bitop3:0xde
	s_add_i32 m0, s39, 0x18000
	v_lshl_add_u64 v[8:9], v[10:11], 0, s[30:31]
	v_lshl_add_u64 v[14:15], s[66:67], 0, v[152:153]
	v_mov_b32_e32 v149, v131
	v_readfirstlane_b32 s100, v0
	s_cmp_lt_u32 s100, 0x100
	s_cbranch_scc1 .Lmy_sp_gate
	s_setprio 1
.Lmy_sp_gate:
	global_load_lds_dwordx4 v[8:9], off
	v_lshl_add_u64 v[8:9], v[12:13], 0, s[30:31]
	s_add_i32 m0, s39, 0x1a000
	s_add_i32 s45, s39, 0x8000
	s_add_i32 s46, s39, 0xa000
	v_lshl_add_u64 v[16:17], s[66:67], 0, v[148:149]
	global_load_lds_dwordx4 v[8:9], off
	v_lshl_add_u64 v[8:9], v[14:15], 0, s[30:31]
	s_mov_b32 m0, s45
	s_add_u32 s6, s68, 0x2080
	global_load_lds_dwordx4 v[8:9], off
	v_lshl_add_u64 v[8:9], v[16:17], 0, s[30:31]
	s_mov_b32 m0, s46
	s_addc_u32 s7, s69, 0
	global_load_lds_dwordx4 v[8:9], off
	s_add_i32 m0, s39, 0x1c000
	v_lshl_add_u64 v[8:9], s[6:7], 0, v[154:155]
	global_load_lds_dwordx4 v[8:9], off
	v_lshl_add_u64 v[8:9], s[6:7], 0, v[150:151]
	s_add_i32 m0, s39, 0x1e000
	s_movk_i32 s6, 0x1e00
	global_load_lds_dwordx4 v[8:9], off
	v_mul_lo_u32 v8, v19, s6
	s_lshl_b32 s6, s8, 6
	v_or3_b32 v169, v8, s6, v18
	v_lshlrev_b32_e32 v8, 13, v6
	v_and_b32_e32 v8, 0xffffc000, v8
	v_lshl_add_u32 v5, v5, 10, v8
	v_and_b32_e32 v6, 1, v6
	v_lshl_or_b32 v5, v6, 6, v5
	v_lshl_add_u32 v156, v7, 1, v5
	v_lshlrev_b32_e32 v5, 13, v2
	v_and_b32_e32 v5, 0xffffc000, v5
	v_readfirstlane_b32 s100, v0
	s_cmp_lt_u32 s100, 0x100
	s_cbranch_scc1 .Lmy_p7_gate
	s_waitcnt vmcnt(10)
	s_barrier
.Lmy_p7_gate:
	s_waitcnt vmcnt(6)
	v_lshl_add_u32 v3, v3, 10, v5
	v_and_b32_e32 v2, 1, v2
	v_lshl_or_b32 v2, v2, 6, v3
	v_mov_b32_e32 v157, v131
	v_lshl_add_u32 v158, v4, 1, v2
	v_mov_b32_e32 v159, v131
	s_mov_b32 s47, 0
	v_add_u32_e32 v170, 0, v20
	s_barrier
	s_waitcnt vmcnt(0)

.LBB0_536:
	s_add_u32 s47, s12, 0x56668000
	s_addc_u32 s50, s13, 0
	s_add_u32 s51, s12, 0x59668000
	s_addc_u32 s53, s13, 0
	s_add_u32 s57, s12, 0x59c68000
	s_addc_u32 s58, s13, 0
	s_add_u32 s59, s12, 0x5bc68000
	v_and_b32_e32 v17, 15, v16
	v_and_b32_e32 v18, 48, v16
	v_lshlrev_b32_e32 v16, 2, v16
	s_addc_u32 s60, s13, 0
	s_and_b32 s5, s7, 3
	v_lshl_or_b32 v144, s6, 6, v17
	s_lshl_b32 s6, s6, 13
	v_lshl_or_b32 v17, v17, 6, v18
	v_and_b32_e32 v16, 32, v16
	s_add_i32 m0, s43, 0x18000
	v_lshl_add_u64 v[8:9], v[8:9], 0, s[30:31]
	v_bitop3_b32 v19, v17, s6, v16 bitop3:0xde
	s_lshl_b32 s6, s5, 12
	v_readfirstlane_b32 s100, v0
	s_cmp_lt_u32 s100, 0x100
	s_cbranch_scc1 .Lmy_sp_g1b
	s_setprio 1
.Lmy_sp_g1b:
	global_load_lds_dwordx4 v[8:9], off
	v_lshl_add_u64 v[6:7], v[6:7], 0, s[30:31]
	s_add_i32 m0, s43, 0x1a000
	s_add_i32 s61, s43, 0x8000
	s_add_i32 s62, s43, 0xa000
	v_bitop3_b32 v145, v17, s6, v16 bitop3:0xde
	global_load_lds_dwordx4 v[6:7], off
	v_lshl_add_u64 v[4:5], v[4:5], 0, s[30:31]
	s_mov_b32 m0, s61
	s_add_u32 s6, s66, 0x4080
	global_load_lds_dwordx4 v[4:5], off
	v_lshl_add_u64 v[2:3], v[2:3], 0, s[30:31]
	s_mov_b32 m0, s62
	s_addc_u32 s7, s67, 0
	global_load_lds_dwordx4 v[2:3], off
	s_add_i32 m0, s43, 0x1c000
	v_lshl_add_u64 v[2:3], s[6:7], 0, v[138:139]
	global_load_lds_dwordx4 v[2:3], off
	v_lshl_add_u64 v[2:3], s[6:7], 0, v[134:135]
	s_add_i32 m0, s43, 0x1e000
	v_lshl_or_b32 v146, s5, 6, v18
	global_load_lds_dwordx4 v[2:3], off
	v_lshlrev_b32_e32 v2, 14, v14
	v_and_b32_e32 v2, 0xffff8000, v2
	v_lshl_add_u32 v2, v13, 11, v2
	v_and_b32_e32 v3, 1, v14
	v_lshl_or_b32 v2, v3, 6, v2
	v_lshl_add_u32 v140, v15, 1, v2
	v_lshlrev_b32_e32 v2, 14, v10
	v_and_b32_e32 v2, 0xffff8000, v2
	v_readfirstlane_b32 s100, v0
	s_cmp_lt_u32 s100, 0x100
	s_cbranch_scc1 .Lmy_p7_g1b
	s_waitcnt vmcnt(10)
	s_barrier
.Lmy_p7_g1b:
	s_waitcnt vmcnt(6)
	v_lshl_add_u32 v2, v11, 11, v2
	v_and_b32_e32 v3, 1, v10
	v_lshl_or_b32 v2, v3, 6, v2
	v_mov_b32_e32 v141, v131
	v_lshl_add_u32 v142, v12, 1, v2
	v_mov_b32_e32 v143, v131
	s_mov_b32 s63, 0
	v_add_u32_e32 v147, 0, v19
	s_mov_b64 s[14:15], s[66:67]
	s_mov_b64 s[12:13], s[18:19]
	s_barrier
	s_branch .LBB0_538

.LBB0_860:
	s_add_u32 s42, s6, 0x45868000
	s_addc_u32 s43, s7, 0
	s_add_u32 s44, s6, 0x63568000
	v_and_b32_e32 v17, 15, v16
	v_and_b32_e32 v18, 48, v16
	v_lshlrev_b32_e32 v16, 2, v16
	s_sext_i32_i8 s17, s8
	s_addc_u32 s45, s7, 0
	s_and_b32 s8, s9, 3
	v_lshl_or_b32 v19, s10, 6, v17
	s_lshl_b32 s6, s10, 13
	v_lshl_or_b32 v17, v17, 6, v18
	v_and_b32_e32 v16, 32, v16
	s_add_i32 m0, s36, 0x18000
	v_lshl_add_u64 v[8:9], v[8:9], 0, s[30:31]
	v_bitop3_b32 v20, v17, s6, v16 bitop3:0xde
	s_lshl_b32 s6, s8, 12
	v_readfirstlane_b32 s100, v0
	s_cmp_lt_u32 s100, 0x100
	s_cbranch_scc1 .Lmy_sp_mrg0
	s_setprio 1
.Lmy_sp_mrg0:
	global_load_lds_dwordx4 v[8:9], off
	v_lshl_add_u64 v[6:7], v[6:7], 0, s[30:31]
	s_add_i32 m0, s36, 0x1a000
	s_add_i32 s46, s36, 0x8000
	s_add_i32 s47, s36, 0xa000
	v_bitop3_b32 v182, v17, s6, v16 bitop3:0xde
	global_load_lds_dwordx4 v[6:7], off
	v_lshl_add_u64 v[4:5], v[4:5], 0, s[30:31]
	s_mov_b32 m0, s46
	s_add_u32 s6, s64, 0x4080
	global_load_lds_dwordx4 v[4:5], off
	v_lshl_add_u64 v[2:3], v[2:3], 0, s[30:31]
	s_mov_b32 m0, s47
	s_addc_u32 s7, s65, 0
	global_load_lds_dwordx4 v[2:3], off
	s_add_i32 m0, s36, 0x1c000
	v_lshl_add_u64 v[2:3], s[6:7], 0, v[164:165]
	global_load_lds_dwordx4 v[2:3], off
	v_lshl_add_u64 v[2:3], s[6:7], 0, v[168:169]
	s_add_i32 m0, s36, 0x1e000
	s_movk_i32 s6, 0x1e00
	global_load_lds_dwordx4 v[2:3], off
	v_mul_lo_u32 v2, v19, s6
	s_lshl_b32 s6, s8, 6
	v_or3_b32 v183, v2, s6, v18
	v_lshlrev_b32_e32 v2, 10, v19
	v_or3_b32 v184, v2, s6, v18
	v_lshlrev_b32_e32 v2, 14, v10
	v_and_b32_e32 v2, 0xffff8000, v2
	v_lshl_add_u32 v2, v11, 11, v2
	v_and_b32_e32 v3, 1, v10
	v_lshl_or_b32 v2, v3, 6, v2
	v_lshl_add_u32 v172, v13, 1, v2
	v_lshlrev_b32_e32 v2, 14, v12
	v_and_b32_e32 v2, 0xffff8000, v2
	v_readfirstlane_b32 s100, v0
	s_cmp_lt_u32 s100, 0x100
	s_cbranch_scc1 .Lmy_p7_mrg0
	s_waitcnt vmcnt(10)
	s_barrier
.Lmy_p7_mrg0:
	s_waitcnt vmcnt(6)
	v_lshl_add_u32 v2, v14, 11, v2
	v_and_b32_e32 v3, 1, v12
	v_lshl_or_b32 v2, v3, 6, v2
	v_mov_b32_e32 v173, v131
	v_lshl_add_u32 v174, v15, 1, v2
	v_mov_b32_e32 v175, v131
	s_mov_b32 s50, 0
	v_add_u32_e32 v185, 0, v20
	s_mov_b64 s[10:11], s[14:15]
	s_mov_b64 s[12:13], s[64:65]
	s_barrier
	s_branch .LBB0_862

.LBB0_952:
	s_add_u32 s39, s8, 0x5ed68000
	v_and_b32_e32 v17, 15, v16
	v_and_b32_e32 v18, 48, v16
	v_lshlrev_b32_e32 v16, 2, v16
	s_sext_i32_i8 s47, s10
	s_addc_u32 s42, s9, 0
	s_and_b32 s10, s12, 3
	v_lshl_or_b32 v19, v17, 6, v18
	s_lshl_b32 s8, s11, 13
	v_and_b32_e32 v16, 32, v16
	s_add_i32 m0, s7, 0x18000
	v_lshl_add_u64 v[8:9], v[8:9], 0, s[30:31]
	v_bitop3_b32 v20, v19, s8, v16 bitop3:0xde
	s_lshl_b32 s8, s10, 12
	v_readfirstlane_b32 s100, v0
	s_cmp_lt_u32 s100, 0x100
	s_cbranch_scc1 .Lmy_sp_wo0
	s_setprio 1
.Lmy_sp_wo0:
	global_load_lds_dwordx4 v[8:9], off
	v_lshl_add_u64 v[6:7], v[6:7], 0, s[30:31]
	s_add_i32 m0, s7, 0x1a000
	s_add_i32 s43, s7, 0x8000
	s_add_i32 s44, s7, 0xa000
	v_bitop3_b32 v144, v19, s8, v16 bitop3:0xde
	global_load_lds_dwordx4 v[6:7], off
	v_lshl_add_u64 v[4:5], v[4:5], 0, s[30:31]
	s_mov_b32 m0, s43
	s_add_u32 s8, s18, 0x4080
	global_load_lds_dwordx4 v[4:5], off
	v_lshl_add_u64 v[2:3], v[2:3], 0, s[30:31]
	s_mov_b32 m0, s44
	s_addc_u32 s9, s19, 0
	global_load_lds_dwordx4 v[2:3], off
	s_add_i32 m0, s7, 0x1c000
	v_lshl_add_u64 v[2:3], s[8:9], 0, v[138:139]
	global_load_lds_dwordx4 v[2:3], off
	v_lshl_add_u64 v[2:3], s[8:9], 0, v[134:135]
	s_add_i32 m0, s7, 0x1e000
	s_lshl_b32 s8, s10, 6
	global_load_lds_dwordx4 v[2:3], off
	v_lshlrev_b32_e32 v2, 10, v17
	v_lshl_or_b32 v2, s11, 16, v2
	v_or3_b32 v145, v2, s8, v18
	v_lshlrev_b32_e32 v2, 14, v13
	v_and_b32_e32 v2, 0xffff8000, v2
	v_lshl_add_u32 v2, v14, 11, v2
	v_and_b32_e32 v3, 1, v13
	v_lshl_or_b32 v2, v3, 6, v2
	v_lshl_add_u32 v140, v15, 1, v2
	v_lshlrev_b32_e32 v2, 14, v10
	v_and_b32_e32 v2, 0xffff8000, v2
	v_readfirstlane_b32 s100, v0
	s_cmp_lt_u32 s100, 0x100
	s_cbranch_scc1 .Lmy_p7_wo0
	s_waitcnt vmcnt(10)
	s_barrier
.Lmy_p7_wo0:
	s_waitcnt vmcnt(6)
	v_lshl_add_u32 v2, v11, 11, v2
	v_and_b32_e32 v3, 1, v10
	v_lshl_or_b32 v2, v3, 6, v2
	v_mov_b32_e32 v141, v131
	v_lshl_add_u32 v142, v12, 1, v2
	v_mov_b32_e32 v143, v131
	s_mov_b32 s45, 0
	v_add_u32_e32 v146, 0, v20
	s_mov_b64 s[14:15], s[18:19]
	s_mov_b64 s[10:11], s[16:17]
	s_barrier

.LBB0_1020:
	s_add_u32 s39, s6, 0x5ed68000
	v_and_b32_e32 v17, 15, v16
	v_and_b32_e32 v18, 48, v16
	v_lshlrev_b32_e32 v16, 2, v16
	s_sext_i32_i8 s47, s8
	s_addc_u32 s42, s7, 0
	s_and_b32 s8, s10, 3
	v_lshl_or_b32 v19, v17, 6, v18
	s_lshl_b32 s6, s9, 13
	v_and_b32_e32 v16, 32, v16
	s_add_i32 m0, s5, 0x18000
	v_lshl_add_u64 v[8:9], v[8:9], 0, s[30:31]
	v_bitop3_b32 v20, v19, s6, v16 bitop3:0xde
	s_lshl_b32 s6, s8, 12
	v_readfirstlane_b32 s100, v0
	s_cmp_lt_u32 s100, 0x100
	s_cbranch_scc1 .Lmy_sp_wo1
	s_setprio 1
.Lmy_sp_wo1:
	global_load_lds_dwordx4 v[8:9], off
	v_lshl_add_u64 v[6:7], v[6:7], 0, s[30:31]
	s_add_i32 m0, s5, 0x1a000
	s_add_i32 s43, s5, 0x8000
	s_add_i32 s44, s5, 0xa000
	v_bitop3_b32 v144, v19, s6, v16 bitop3:0xde
	global_load_lds_dwordx4 v[6:7], off
	v_lshl_add_u64 v[4:5], v[4:5], 0, s[30:31]
	s_mov_b32 m0, s43
	s_add_u32 s6, s16, 0x4080
	global_load_lds_dwordx4 v[4:5], off
	v_lshl_add_u64 v[2:3], v[2:3], 0, s[30:31]
	s_mov_b32 m0, s44
	s_addc_u32 s7, s17, 0
	global_load_lds_dwordx4 v[2:3], off
	s_add_i32 m0, s5, 0x1c000
	v_lshl_add_u64 v[2:3], s[6:7], 0, v[132:133]
	global_load_lds_dwordx4 v[2:3], off
	v_lshl_add_u64 v[2:3], s[6:7], 0, v[136:137]
	s_add_i32 m0, s5, 0x1e000
	s_lshl_b32 s6, s8, 6
	global_load_lds_dwordx4 v[2:3], off
	v_lshlrev_b32_e32 v2, 10, v17
	v_lshl_or_b32 v2, s9, 16, v2
	v_or3_b32 v145, v2, s6, v18
	v_lshlrev_b32_e32 v2, 14, v10
	v_and_b32_e32 v2, 0xffff8000, v2
	v_lshl_add_u32 v2, v11, 11, v2
	v_and_b32_e32 v3, 1, v10
	v_lshl_or_b32 v2, v3, 6, v2
	v_lshl_add_u32 v140, v13, 1, v2
	v_lshlrev_b32_e32 v2, 14, v12
	v_and_b32_e32 v2, 0xffff8000, v2
	v_readfirstlane_b32 s100, v0
	s_cmp_lt_u32 s100, 0x100
	s_cbranch_scc1 .Lmy_p7_wo1
	s_waitcnt vmcnt(10)
	s_barrier
.Lmy_p7_wo1:
	s_waitcnt vmcnt(6)
	v_lshl_add_u32 v2, v14, 11, v2
	v_and_b32_e32 v3, 1, v12
	v_lshl_or_b32 v2, v3, 6, v2
	v_mov_b32_e32 v141, v131
	v_lshl_add_u32 v142, v15, 1, v2
	v_mov_b32_e32 v143, v131
	s_mov_b32 s45, 0
	v_add_u32_e32 v146, 0, v20
	s_mov_b64 s[10:11], s[14:15]
	s_mov_b64 s[12:13], s[16:17]
	s_barrier

.LBB0_1094:
	s_add_u32 s42, s4, 0x45868000
	s_addc_u32 s43, s5, 0
	s_add_u32 s44, s4, 0x63568000
	v_and_b32_e32 v17, 15, v16
	v_and_b32_e32 v18, 48, v16
	v_lshlrev_b32_e32 v16, 2, v16
	s_sext_i32_i8 s15, s6
	s_addc_u32 s45, s5, 0
	s_and_b32 s6, s7, 3
	v_lshl_or_b32 v19, s8, 6, v17
	s_lshl_b32 s4, s8, 13
	v_lshl_or_b32 v17, v17, 6, v18
	v_and_b32_e32 v16, 32, v16
	s_add_i32 m0, s36, 0x18000
	v_lshl_add_u64 v[8:9], v[8:9], 0, s[30:31]
	v_bitop3_b32 v20, v17, s4, v16 bitop3:0xde
	s_lshl_b32 s4, s6, 12
	v_readfirstlane_b32 s100, v0
	s_cmp_lt_u32 s100, 0x100
	s_cbranch_scc1 .Lmy_sp_mrgL
	s_setprio 1
.Lmy_sp_mrgL:
	global_load_lds_dwordx4 v[8:9], off
	v_lshl_add_u64 v[6:7], v[6:7], 0, s[30:31]
	s_add_i32 m0, s36, 0x1a000
	s_add_i32 s46, s36, 0x8000
	s_add_i32 s47, s36, 0xa000
	v_bitop3_b32 v182, v17, s4, v16 bitop3:0xde
	global_load_lds_dwordx4 v[6:7], off
	v_lshl_add_u64 v[4:5], v[4:5], 0, s[30:31]
	s_mov_b32 m0, s46
	s_add_u32 s4, s62, 0x4080
	global_load_lds_dwordx4 v[4:5], off
	v_lshl_add_u64 v[2:3], v[2:3], 0, s[30:31]
	s_mov_b32 m0, s47
	s_addc_u32 s5, s63, 0
	global_load_lds_dwordx4 v[2:3], off
	s_add_i32 m0, s36, 0x1c000
	v_lshl_add_u64 v[2:3], s[4:5], 0, v[164:165]
	global_load_lds_dwordx4 v[2:3], off
	v_lshl_add_u64 v[2:3], s[4:5], 0, v[168:169]
	s_add_i32 m0, s36, 0x1e000
	s_movk_i32 s4, 0x1e00
	global_load_lds_dwordx4 v[2:3], off
	v_mul_lo_u32 v2, v19, s4
	s_lshl_b32 s4, s6, 6
	v_or3_b32 v183, v2, s4, v18
	v_lshlrev_b32_e32 v2, 10, v19
	v_or3_b32 v184, v2, s4, v18
	v_lshlrev_b32_e32 v2, 14, v10
	v_and_b32_e32 v2, 0xffff8000, v2
	v_lshl_add_u32 v2, v11, 11, v2
	v_and_b32_e32 v3, 1, v10
	v_lshl_or_b32 v2, v3, 6, v2
	v_lshl_add_u32 v172, v13, 1, v2
	v_lshlrev_b32_e32 v2, 14, v12
	v_and_b32_e32 v2, 0xffff8000, v2
	v_readfirstlane_b32 s100, v0
	s_cmp_lt_u32 s100, 0x100
	s_cbranch_scc1 .Lmy_p7_mrgL
	s_waitcnt vmcnt(10)
	s_barrier
.Lmy_p7_mrgL:
	s_waitcnt vmcnt(6)
	v_lshl_add_u32 v2, v14, 11, v2
	v_and_b32_e32 v3, 1, v12
	v_lshl_or_b32 v2, v3, 6, v2
	v_mov_b32_e32 v173, v131
	v_lshl_add_u32 v174, v15, 1, v2
	v_mov_b32_e32 v175, v131
	s_mov_b32 s50, 0
	v_add_u32_e32 v185, 0, v20
	s_mov_b64 s[8:9], s[12:13]
	s_mov_b64 s[10:11], s[62:63]
	s_barrier
	s_branch .LBB0_1096

.LBB0_1415:
	s_lshl_b32 s59, s8, 7
	v_and_b32_e32 v17, 15, v16
	v_lshrrev_b32_e32 v18, 1, v16
	s_add_u32 s47, s4, 0x45868000
	v_and_b32_e32 v18, 24, v18
	v_lshlrev_b32_e32 v19, 6, v17
	v_lshlrev_b32_e32 v16, 2, v16
	s_addc_u32 s50, s5, 0
	v_lshl_or_b32 v19, v18, 1, v19
	s_lshl_b32 s4, s6, 13
	v_and_b32_e32 v16, 32, v16
	v_bitop3_b32 v20, v19, s4, v16 bitop3:0xde
	s_lshl_b32 s4, s7, 5
	s_and_b32 s7, s4, 0x60
	s_add_i32 m0, s43, 0x18000
	v_lshl_add_u64 v[8:9], v[8:9], 0, s[30:31]
	s_lshl_b32 s4, s7, 7
	v_readfirstlane_b32 s100, v0
	s_cmp_lt_u32 s100, 0x100
	s_cbranch_scc1 .Lmy_sp_up
	s_setprio 1
.Lmy_sp_up:
	global_load_lds_dwordx4 v[8:9], off
	v_lshl_add_u64 v[6:7], v[6:7], 0, s[30:31]
	s_add_i32 m0, s43, 0x1a000
	s_add_i32 s51, s43, 0x8000
	s_add_i32 s53, s43, 0xa000
	v_bitop3_b32 v168, v19, s4, v16 bitop3:0xde
	global_load_lds_dwordx4 v[6:7], off
	v_lshl_add_u64 v[4:5], v[4:5], 0, s[30:31]
	s_mov_b32 m0, s51
	s_add_u32 s4, s60, 0x2080
	global_load_lds_dwordx4 v[4:5], off
	v_lshl_add_u64 v[2:3], v[2:3], 0, s[30:31]
	s_mov_b32 m0, s53
	s_addc_u32 s5, s61, 0
	global_load_lds_dwordx4 v[2:3], off
	s_add_i32 m0, s43, 0x1c000
	v_lshl_add_u64 v[2:3], s[4:5], 0, v[154:155]
	global_load_lds_dwordx4 v[2:3], off
	v_lshl_add_u64 v[2:3], s[4:5], 0, v[150:151]
	s_add_i32 m0, s43, 0x1e000
	s_sub_i32 s4, 0, s1
	global_load_lds_dwordx4 v[2:3], off
	v_lshlrev_b32_e32 v2, 11, v17
	v_lshl_or_b32 v2, s6, 17, v2
	v_or3_b32 v169, s7, v2, v18
	v_cvt_f32_ubyte0_e32 v2, s1
	v_rcp_iflag_f32_e32 v2, v2
	v_and_b32_e32 v3, 1, v14
	v_readfirstlane_b32 s100, v0
	s_cmp_lt_u32 s100, 0x100
	s_cbranch_scc1 .Lmy_p7_up
	s_waitcnt vmcnt(10)
	s_barrier
.Lmy_p7_up:
	s_waitcnt vmcnt(6)
	s_mov_b32 s57, 0
	v_mul_f32_e32 v2, 0x4f7ffffe, v2
	v_cvt_u32_f32_e32 v2, v2
	v_mov_b32_e32 v157, v131
	v_mov_b32_e32 v159, v131
	v_add_u32_e32 v170, 0, v20
	v_readfirstlane_b32 s5, v2
	v_lshlrev_b32_e32 v2, 13, v14
	v_and_b32_e32 v2, 0xffffc000, v2
	v_lshl_add_u32 v2, v13, 10, v2
	v_lshl_or_b32 v2, v3, 6, v2
	v_lshl_add_u32 v156, v15, 1, v2
	v_lshlrev_b32_e32 v2, 13, v10
	v_and_b32_e32 v2, 0xffffc000, v2
	s_mul_i32 s4, s4, s5
	v_lshl_add_u32 v2, v11, 10, v2
	v_and_b32_e32 v3, 1, v10
	s_mul_hi_u32 s4, s5, s4
	v_lshl_or_b32 v2, v3, 6, v2
	s_add_i32 s58, s5, s4
	v_lshl_add_u32 v158, v12, 1, v2
	s_barrier
	s_waitcnt vmcnt(0)

.LBB0_1479:
	s_add_u32 s46, s4, 0x67d68000
	v_and_b32_e32 v17, 15, v16
	v_and_b32_e32 v18, 48, v16
	v_lshlrev_b32_e32 v16, 2, v16
	s_addc_u32 s47, s5, 0
	s_and_b32 s7, s7, 3
	s_lshl_b32 s4, s6, 13
	v_lshl_or_b32 v19, v17, 6, v18
	v_and_b32_e32 v16, 32, v16
	s_add_i32 m0, s17, 0x18000
	v_lshl_add_u64 v[8:9], v[8:9], 0, s[30:31]
	v_bitop3_b32 v20, v19, s4, v16 bitop3:0xde
	s_lshl_b32 s4, s7, 12
	v_readfirstlane_b32 s100, v0
	s_cmp_lt_u32 s100, 0x100
	s_cbranch_scc1 .Lmy_sp_down
	s_setprio 1
.Lmy_sp_down:
	global_load_lds_dwordx4 v[8:9], off
	v_lshl_add_u64 v[6:7], v[6:7], 0, s[30:31]
	s_add_i32 m0, s17, 0x1a000
	s_add_i32 s50, s17, 0x8000
	s_add_i32 s51, s17, 0xa000
	v_bitop3_b32 v168, v19, s4, v16 bitop3:0xde
	global_load_lds_dwordx4 v[6:7], off
	v_lshl_add_u64 v[4:5], v[4:5], 0, s[30:31]
	s_mov_b32 m0, s50
	s_add_u32 s4, s64, 0x4080
	global_load_lds_dwordx4 v[4:5], off
	v_lshl_add_u64 v[2:3], v[2:3], 0, s[30:31]
	s_mov_b32 m0, s51
	s_addc_u32 s5, s65, 0
	global_load_lds_dwordx4 v[2:3], off
	s_add_i32 m0, s17, 0x1c000
	v_lshl_add_u64 v[2:3], s[4:5], 0, v[154:155]
	global_load_lds_dwordx4 v[2:3], off
	v_lshl_add_u64 v[2:3], s[4:5], 0, v[150:151]
	s_add_i32 m0, s17, 0x1e000
	s_lshl_b32 s4, s7, 6
	global_load_lds_dwordx4 v[2:3], off
	v_lshlrev_b32_e32 v2, 10, v17
	v_lshl_or_b32 v2, s6, 16, v2
	v_or3_b32 v169, v2, s4, v18
	v_lshlrev_b32_e32 v2, 14, v14
	v_and_b32_e32 v2, 0xffff8000, v2
	v_lshl_add_u32 v2, v13, 11, v2
	v_and_b32_e32 v3, 1, v14
	v_lshl_or_b32 v2, v3, 6, v2
	v_lshl_add_u32 v156, v15, 1, v2
	v_lshlrev_b32_e32 v2, 14, v10
	v_and_b32_e32 v2, 0xffff8000, v2
	v_readfirstlane_b32 s100, v0
	s_cmp_lt_u32 s100, 0x100
	s_cbranch_scc1 .Lmy_p7_down
	s_waitcnt vmcnt(10)
	s_barrier
.Lmy_p7_down:
	s_waitcnt vmcnt(6)
	v_lshl_add_u32 v2, v11, 11, v2
	v_and_b32_e32 v3, 1, v10
	v_lshl_or_b32 v2, v3, 6, v2
	v_mov_b32_e32 v157, v131
	v_lshl_add_u32 v158, v12, 1, v2
	v_mov_b32_e32 v159, v131
	s_mov_b32 s53, 0
	v_add_u32_e32 v170, 0, v20
	s_barrier
